# k42: k40 with the P2 tile split retuned after the barrier changes: GEMM workgroups convert the last 640 tiles (5 each) instead of 768
# speedup vs baseline: 1.0158x; 1.0030x over previous
; __global__ void __launch_bounds__(NWAVES * 64, 2) fwd_kernel(Args args) {
;     ...
;                 T8_RUN(vcu, G, (G == 256) ? U_TOT - T8_NMOVE : U_TOT);
;     ...
;         } else { constexpr int TRB = 256 * 144; T8_CONSTS; T8_RUN(U_TOT - T8_NMOVE + (slot2 - T8_GS) * 8 + xcd2, (32 - T8_GS) * 8, U_TOT); }
.La3c_done:
	s_movk_i32 s98, 0x3040
	s_movk_i32 s99, 0x2fc0
	s_movk_i32 s100, 0x2f40
	s_movk_i32 s101, 0x740

; __global__ void __launch_bounds__(NWAVES * 64, 2) fwd_kernel(Args args) {
;     ...
;                 T8_RUN(vcu, G, (G == 256) ? U_TOT - T8_NMOVE : U_TOT);
;     ...
;         } else { constexpr int TRB = 256 * 144; T8_CONSTS; T8_RUN(U_TOT - T8_NMOVE + (slot2 - T8_GS) * 8 + xcd2, (32 - T8_GS) * 8, U_TOT); }
.La3g_done:
	v_readlane_b32 s4, v254, 1
	v_readlane_b32 s5, v254, 2
	s_movk_i32 s98, 0x32c0
	s_movk_i32 s99, 0x3240
	s_movk_i32 s100, 0x31c0
	s_movk_i32 s101, 0x3040
	s_load_dwordx2 s[8:9], s[4:5], 0xf8
	s_branch .Lp2_conv_entry
